# adds P5a->P5b seam without vmcnt(0) drain
# baseline (speedup 1.0000x reference)
; #define PG8_SETVO(dst, u) do { _Pragma("unroll") for (int _h = 0; _h < 2; ++_h) _Pragma("unroll") for (int _i = 0; _i < 2; ++_i) { \
;         if constexpr (GATHER) { int R_, C_; stage_rc(tid * 16 + _i * 8192, R_, C_); dst[_h][_i] = (unsigned)(S.arow(u, R_ + HALF * _h) * K + C_) * 2u; } \
;         else dst[_h][_i] = voffA[_i] + (unsigned)_h * (unsigned)(HALF * K * 2); } } while (0)
; #define PG8_STAGE(bufoff, gbase, voff) do { _Pragma("unroll") for (int _i = 0; _i < 2; ++_i) \
;         __builtin_amdgcn_global_load_lds((const unsigned*)((const char*)(gbase) + (voff)[_i]), (PG8_LAS unsigned*)(lds + (bufoff) + ldsw + _i * 8192), 16, 0, 0); } while (0)
; #define PG8_WAIT_V(n) asm volatile("s_waitcnt vmcnt(" #n ")" ::: "memory")
; #define PG8_BAR __builtin_amdgcn_s_barrier()
; #define VM_WAIT() asm volatile("s_waitcnt vmcnt(0)" ::: "memory")
; template <class Epi, class Sched, bool ALIGN_EPI = false, bool SP2 = false, bool F8 = false, bool GATHER = false>
; __device__ __forceinline__ void gemm_phase(PG8_LAS unsigned char* lds, const Gemm g, const Sched& S, const Epi& E) {
;     ...
;     const char* cA = (const char*)g.A + (GATHER ? (size_t)0 : (size_t)cur.pm * tstep); const char* cB = (const char*)g.Bt + (size_t)cur.pn * tstep;
;     PG8_SETVO(vo, cur);
;     S.a_ready(cur);
;     if constexpr (SP2) {
;         PG8_STAGE(PG8_SB(0, 0), cB, voffB); PG8_STAGE(PG8_SB(0, 1), cB + hstep, voffB); PG8_STAGE(PG8_SA(0, 0), cA, vo[0]); PG8_STAGE(PG8_SA(0, 1), cA, vo[1]);
;         if (wr == 1) PG8_BAR;
;         PG8_WAIT_V(2); PG8_BAR;
;         PG8_STAGE(PG8_SB(1, 0), cB + kstep, voffB); PG8_STAGE(PG8_SA(1, 0), cA + kstep, vo[0]); PG8_STAGE(PG8_SB(1, 1), cB + hstep + kstep, voffB);
; __global__ void __launch_bounds__(NWAVES * 64, 2) fwd(Args args) {
;     ...
;           pg8::gemm_phase<pg8::EpiM1, pg8::StaticOrder, AL, SP, P5_F8>(F.lds + RING_OFF, g, S, E); }
;         VM_WAIT(); __syncthreads();
;         { pg8::Gemm g{WSP(bf16, WS_YB), WSP(bf16, WS_WBT), T, DM, P5_F8 ? 512 : 1024}; pg8::StaticOrder S; S.init(T, DM, F.G, (int)blockIdx.x);
;           if constexpr (P6_F8) { pg8::EpiMerged E{WSP(bf16, WS_M1), WSP(bf16, WS_QKV) + C_GB, NQKV, WSP(unsigned char, WS_MG)};
;             pg8::gemm_phase<pg8::EpiMerged, pg8::StaticOrder, AL, SP, P5_F8>(F.lds + RING_OFF, g, S, E); }
.LBB0_736:
	s_nop 0
	s_barrier
.LBB0_737:
	s_nop 0
	v_mov_b32_e32 v10, v0
	s_waitcnt lgkmcnt(0)
	s_barrier
	s_andn2_b64 vcc, exec, s[18:19]
	v_readfirstlane_b32 s5, v10
	s_cbranch_vccnz .LBB0_757
	v_lshlrev_b32_e32 v2, 4, v10
	v_add_u32_e32 v3, 0x2000, v2
	v_ashrrev_i32_e32 v4, 31, v3
	v_lshrrev_b32_e32 v4, 22, v4
	v_add_u32_e32 v4, v3, v4
	v_ashrrev_i32_e32 v11, 10, v4
	v_mul_i32_i24_e32 v4, 0x400, v11
	v_sub_u32_e32 v3, v3, v4
	v_lshrrev_b32_e32 v4, 4, v3
	v_bitop3_b32 v3, v4, v3, 32 bitop3:0x6c
	v_ashrrev_i32_e32 v4, 31, v3
	v_lshrrev_b32_e32 v4, 26, v4
	v_add_u32_e32 v4, v3, v4
	v_lshlrev_b32_e32 v5, 3, v11
	v_ashrrev_i32_e32 v12, 6, v4
	v_and_b32_e32 v5, -16, v5
	v_add_u32_e32 v5, v12, v5
	v_and_b32_e32 v6, 3, v12
	s_mov_b32 s4, 0x3fffe0
	v_lshrrev_b32_e32 v7, 2, v5
	v_lshlrev_b32_e32 v8, 1, v5
	v_and_b32_e32 v4, 0xc0, v4
	v_and_or_b32 v6, v5, s4, v6
	v_and_b32_e32 v7, 4, v7
	v_and_b32_e32 v8, 24, v8
	v_sub_u32_e32 v3, v3, v4
	v_mov_b32_e32 v4, 1
	v_or3_b32 v6, v6, v7, v8
	v_lshlrev_b32_e32 v7, 5, v11
	v_ashrrev_i16_sdwa v3, v4, sext(v3) dst_sel:DWORD dst_unused:UNUSED_PAD src0_sel:DWORD src1_sel:BYTE_0
	v_and_b32_e32 v7, 32, v7
	v_bfe_i32 v13, v3, 0, 16
	v_add_lshl_u32 v3, v7, v13, 1
	v_lshl_add_u32 v162, v6, 10, v3
	v_lshl_add_u32 v164, v5, 10, v3
	v_bfe_i32 v3, v10, 27, 1
	v_lshrrev_b32_e32 v3, 22, v3
	v_add_u32_e32 v3, v2, v3
	v_and_b32_e32 v3, 0xfffffc00, v3
	v_sub_u32_e32 v2, v2, v3
	s_ashr_i32 s18, s5, 6
	v_lshrrev_b32_e32 v3, 4, v2
	v_ashrrev_i32_e32 v5, 31, v10
	s_ashr_i32 s38, s5, 8
	s_lshl_b32 s2, s18, 10
	v_bitop3_b32 v2, v3, v2, 32 bitop3:0x6c
	v_lshrrev_b32_e32 v5, 26, v5
	s_add_u32 s3, s30, 0x1b200000
	v_ashrrev_i32_e32 v3, 31, v2
	v_add_u32_e32 v5, v10, v5
	s_addc_u32 s10, s31, 0
	v_lshrrev_b32_e32 v3, 26, v3
	v_ashrrev_i32_e32 v15, 6, v5
	s_add_u32 s11, s30, 0x3000000
	v_add_u32_e32 v3, v2, v3
	v_lshlrev_b32_e32 v5, 3, v15
	s_addc_u32 s33, s31, 0
	v_ashrrev_i32_e32 v14, 6, v3
	v_and_b32_e32 v5, -16, v5
	v_add_u32_e32 v5, v14, v5
	v_and_b32_e32 v6, 3, v14
	s_and_b64 s[14:15], s[14:15], exec
	v_and_or_b32 v6, v5, s4, v6
	s_cselect_b32 s4, s43, s35
	s_add_i32 s4, s4, s34
	s_ashr_i32 s14, s4, 31
	s_lshr_b32 s14, s14, 26
	s_add_i32 s14, s4, s14
	s_ashr_i32 s15, s14, 6
	s_andn2_b32 s14, s14, 63
	s_sub_i32 s14, s4, s14
	s_bfe_i32 s4, s14, 0x80000
	s_bfe_u32 s4, s4, 0x3000c
	s_add_i32 s19, s14, s4
	s_bfe_i32 s4, s19, 0x80000
	s_and_b32 s19, s19, 0xf8
	s_sub_i32 s14, s14, s19
	s_lshl_b32 s15, s15, 3
	s_sext_i32_i16 s4, s4
	s_sext_i32_i8 s14, s14
	v_lshrrev_b32_e32 v7, 2, v5
	v_lshlrev_b32_e32 v8, 1, v5
	v_and_b32_e32 v3, 0xc0, v3
	s_lshr_b32 s4, s4, 3
	s_add_i32 s56, s15, s14
	v_and_b32_e32 v7, 4, v7
	v_and_b32_e32 v8, 24, v8
	v_sub_u32_e32 v2, v2, v3
	s_ashr_i32 s57, s56, 31
	s_bfe_i64 s[22:23], s[4:5], 0x100000
	v_or3_b32 v6, v6, v7, v8
	v_lshlrev_b32_e32 v7, 5, v15
	v_ashrrev_i16_sdwa v2, v4, sext(v2) dst_sel:DWORD dst_unused:UNUSED_PAD src0_sel:DWORD src1_sel:BYTE_0
	s_lshl_b64 s[14:15], s[56:57], 18
	s_lshl_b64 s[22:23], s[22:23], 18
	v_and_b32_e32 v7, 32, v7
	v_bfe_i32 v16, v2, 0, 16
	s_add_u32 s60, s11, s22
	v_add_lshl_u32 v2, v7, v16, 1
	s_addc_u32 s61, s33, s23
	s_add_i32 s34, s2, 0
	v_lshl_add_u32 v166, v6, 10, v2
	s_add_i32 m0, s34, 0x10000
	v_lshl_add_u32 v168, v5, 10, v2
	global_load_lds_dwordx4 v166, s[60:61]
	s_add_i32 m0, s34, 0x12000
	s_add_u32 s22, s60, 0x20000
	global_load_lds_dwordx4 v162, s[60:61]
	s_addc_u32 s23, s61, 0
	s_add_i32 m0, s34, 0x14000
	v_add_u32_e32 v170, 0x20000, v168
	global_load_lds_dwordx4 v166, s[22:23]
	s_add_i32 m0, s34, 0x16000
	s_add_u32 s58, s3, s14
	global_load_lds_dwordx4 v162, s[22:23]
	s_addc_u32 s59, s10, s15
	s_mov_b32 m0, s34
	s_add_i32 s35, s34, 0x2000
	global_load_lds_dwordx4 v168, s[58:59]
	s_mov_b32 m0, s35
	s_add_i32 s41, s34, 0x4000
	global_load_lds_dwordx4 v164, s[58:59]
	s_mov_b32 m0, s41
	s_add_i32 s48, s34, 0x6000
	v_add_u32_e32 v172, 0x20000, v164
	global_load_lds_dwordx4 v170, s[58:59]
	s_mov_b32 m0, s48
	v_mov_b32_e32 v167, 0
	global_load_lds_dwordx4 v172, s[58:59]
	v_mov_b32_e32 v163, v167
	v_mov_b32_e32 v169, v167
	v_mov_b32_e32 v165, v167
	s_cmp_eq_u32 s38, 1
	s_mov_b32 s40, 0x20000
	s_mov_b32 s49, 0
	v_lshl_add_u64 v[8:9], s[60:61], 0, v[166:167]
	v_lshl_add_u64 v[6:7], s[60:61], 0, v[162:163]
	v_lshl_add_u64 v[2:3], s[58:59], 0, v[168:169]
	s_cselect_b64 s[14:15], -1, 0
	s_cmp_lg_u32 s38, 1
	v_lshl_add_u64 v[4:5], s[58:59], 0, v[164:165]
	s_cbranch_scc1 .LBB0_740
	s_barrier
